# baseline (speedup 1.0000x reference)
.LBB3_9:
	v_add_u32_e32 v138, s48, v207
	ds_read_b64_tr_b16 v[156:157], v138 offset:24576
	ds_read_b64_tr_b16 v[158:159], v138 offset:25088
	v_add_f32_e32 v120, v80, v81
	s_waitcnt lgkmcnt(3)
	v_mfma_scale_f32_32x32x64_f8f6f4 v[48:63], v[112:119], v[96:103], v[48:63], v219, v220 op_sel_hi:[0,0,0]
	v_add_f32_e32 v112, v82, v120
	v_add_f32_e32 v112, v83, v112
	v_add_f32_e32 v112, v84, v112
	v_add_f32_e32 v116, v85, v112
	v_cvt_pk_f16_f32 v132, v80, v81
	v_cvt_pk_f16_f32 v133, v82, v83
	ds_read_b64_tr_b16 v[112:113], v138 offset:28672
	ds_read_b64_tr_b16 v[114:115], v138 offset:29184
	v_add_f32_e32 v80, v86, v116
	v_add_f32_e32 v80, v87, v80
	v_add_f32_e32 v80, v88, v80
	v_add_f32_e32 v80, v89, v80
	v_cvt_pk_f16_f32 v134, v84, v85
	v_cvt_pk_f16_f32 v135, v86, v87
	s_waitcnt lgkmcnt(4)
	v_mfma_scale_f32_32x32x64_f8f6f4 v[32:47], v[104:111], v[96:103], v[32:47], v219, v220 op_sel_hi:[0,0,0]
	v_lshl_add_u64 v[186:187], v[164:165], 0, s[2:3]
	v_lshl_add_u64 v[228:229], v[186:187], 0, s[12:13]
	v_lshl_add_u64 v[228:229], v[228:229], 0, s[62:63]
	s_add_i32 m0, s36, s65
	s_nop 0
	global_load_lds_dwordx4 v[228:229], off nt
	ds_read_b64_tr_b16 v[104:105], v138 offset:25600
	ds_read_b64_tr_b16 v[106:107], v138 offset:26112
	v_add_f32_e32 v80, v90, v80
	v_add_f32_e32 v80, v91, v80
	v_add_f32_e32 v80, v92, v80
	v_add_f32_e32 v80, v93, v80
	v_cvt_pk_f16_f32 v128, v88, v89
	v_cvt_pk_f16_f32 v129, v90, v91
	ds_read_b64_tr_b16 v[152:153], v138 offset:29696
	ds_read_b64_tr_b16 v[154:155], v138 offset:30208
	v_lshl_add_u64 v[188:189], v[178:179], 0, s[2:3]
	v_lshl_add_u64 v[228:229], v[188:189], 0, s[12:13]
	v_lshl_add_u64 v[228:229], v[228:229], 0, s[62:63]
	s_add_i32 m0, s30, s65
	s_nop 0
	global_load_lds_dwordx4 v[228:229], off nt
	v_add_f32_e32 v80, v94, v80
	v_add_f32_e32 v80, v95, v80
	v_add_f32_e32 v80, v64, v80
	v_add_f32_e32 v80, v65, v80
	v_cvt_pk_f16_f32 v130, v92, v93
	v_cvt_pk_f16_f32 v131, v94, v95
	ds_read_b64_tr_b16 v[148:149], v138 offset:26624
	ds_read_b64_tr_b16 v[150:151], v138 offset:27136
	v_add_f32_e32 v80, v66, v80
	v_add_f32_e32 v80, v67, v80
	v_add_f32_e32 v80, v68, v80
	v_add_f32_e32 v80, v69, v80
	v_cvt_pk_f16_f32 v124, v64, v65
	v_cvt_pk_f16_f32 v125, v66, v67
	ds_read_b64_tr_b16 v[144:145], v138 offset:30720
	ds_read_b64_tr_b16 v[146:147], v138 offset:31232
	v_lshl_add_u64 v[190:191], v[176:177], 0, s[2:3]
	v_lshl_add_u64 v[228:229], v[190:191], 0, s[12:13]
	v_lshl_add_u64 v[228:229], v[228:229], 0, s[62:63]
	s_add_i32 m0, s31, s65
	s_nop 0
	global_load_lds_dwordx4 v[228:229], off nt
	v_add_f32_e32 v64, v70, v80
	v_add_f32_e32 v64, v71, v64
	v_add_f32_e32 v64, v72, v64
	v_add_f32_e32 v64, v73, v64
	v_cvt_pk_f16_f32 v126, v68, v69
	v_cvt_pk_f16_f32 v127, v70, v71
	ds_read_b64_tr_b16 v[140:141], v138 offset:27648
	ds_read_b64_tr_b16 v[142:143], v138 offset:28160
	v_add_f32_e32 v64, v74, v64
	v_add_f32_e32 v64, v75, v64
	v_add_f32_e32 v64, v76, v64
	v_add_f32_e32 v64, v77, v64
	v_cvt_pk_f16_f32 v120, v72, v73
	v_cvt_pk_f16_f32 v121, v74, v75
	ds_read_b64_tr_b16 v[136:137], v138 offset:31744
	ds_read_b64_tr_b16 v[138:139], v138 offset:32256
	v_lshl_add_u64 v[192:193], v[174:175], 0, s[2:3]
	v_lshl_add_u64 v[228:229], v[192:193], 0, s[12:13]
	v_lshl_add_u64 v[228:229], v[228:229], 0, s[62:63]
	s_add_i32 m0, s40, s65
	s_nop 0
	global_load_lds_dwordx4 v[228:229], off nt
	v_add_f32_e32 v64, v78, v64
	v_add_f32_e32 v64, v79, v64
	v_add_f32_e32 v108, 0, v64
	v_cvt_pk_f16_f32 v122, v76, v77
	v_cvt_pk_f16_f32 v123, v78, v79
	s_nop 1
	s_nop 0
	v_add_f32_e32 v185, v185, v108
	v_max_f32_e32 v108, v49, v49
	v_max_f32_e32 v109, v48, v48
	v_max_f32_e32 v108, v109, v108
	v_max3_f32 v109, v50, v51, v33
	v_max3_f32 v108, v108, v32, v34
	v_max3_f32 v108, v108, v35, v52
	v_max3_f32 v109, v109, v54, v55
	v_max3_f32 v108, v108, v53, v36
	v_max3_f32 v109, v109, v38, v39
	v_max3_f32 v108, v108, v37, v56
	v_max3_f32 v109, v109, v58, v59
	v_add_u32_e32 v221, v222, v223
	v_max3_f32 v108, v108, v57, v40
	v_max3_f32 v109, v109, v42, v43
	ds_read_b128 v[80:83], v221
	ds_read_b128 v[64:67], v161
	ds_read_b128 v[84:87], v184
	ds_read_b128 v[68:71], v211
	ds_read_b128 v[88:91], v212
	ds_read_b128 v[72:75], v213
	ds_read_b128 v[92:95], v214
	ds_read_b128 v[76:79], v215
	v_max3_f32 v108, v108, v41, v60
	v_max3_f32 v109, v109, v62, v63
	v_max3_f32 v108, v108, v61, v44
	v_max3_f32 v109, v109, v46, v47
	v_max3_f32 v108, v108, v45, v109
	v_mov_b32_e32 v109, v108
	s_nop 1
	v_permlane32_swap_b32_e32 v108, v109
	v_max_f32_e32 v109, v109, v109
	v_max_f32_e32 v108, v108, v108
	v_max_f32_e32 v108, v108, v109
	v_fma_f32 v108, v108, s39, -v208
	v_cmp_lt_f32_e32 vcc, s46, v108
	s_cmp_lg_u64 vcc, 0
	s_cselect_b64 s[26:27], -1, 0
	s_cbranch_vccnz .LBB3_21

.LBB3_14:
	v_add_u32_e32 v138, s47, v207
	ds_read_b64_tr_b16 v[156:157], v138 offset:24576
	ds_read_b64_tr_b16 v[158:159], v138 offset:25088
	v_add_f32_e32 v120, v48, v49
	s_waitcnt lgkmcnt(4)
	v_mfma_scale_f32_32x32x64_f8f6f4 v[80:95], v[112:119], v[96:103], v[80:95], v219, v220 op_sel_hi:[0,0,0]
	v_add_f32_e32 v112, v50, v120
	v_add_f32_e32 v112, v51, v112
	v_add_f32_e32 v112, v52, v112
	v_add_f32_e32 v116, v53, v112
	v_cvt_pk_f16_f32 v132, v48, v49
	v_cvt_pk_f16_f32 v133, v50, v51
	ds_read_b64_tr_b16 v[112:113], v138 offset:28672
	ds_read_b64_tr_b16 v[114:115], v138 offset:29184
	v_add_f32_e32 v48, v54, v116
	v_add_f32_e32 v48, v55, v48
	v_add_f32_e32 v48, v56, v48
	v_add_f32_e32 v48, v57, v48
	v_cvt_pk_f16_f32 v134, v52, v53
	v_cvt_pk_f16_f32 v135, v54, v55
	s_waitcnt lgkmcnt(4)
	v_mfma_scale_f32_32x32x64_f8f6f4 v[64:79], v[104:111], v[96:103], v[64:79], v219, v220 op_sel_hi:[0,0,0]
	v_lshl_add_u64 v[228:229], v[186:187], 0, s[22:23]
	v_lshl_add_u64 v[228:229], v[228:229], 0, s[62:63]
	s_add_i32 m0, s36, s64
	s_nop 0
	global_load_lds_dwordx4 v[228:229], off nt
	ds_read_b64_tr_b16 v[104:105], v138 offset:25600
	ds_read_b64_tr_b16 v[106:107], v138 offset:26112
	v_add_f32_e32 v48, v58, v48
	v_add_f32_e32 v48, v59, v48
	v_add_f32_e32 v48, v60, v48
	v_add_f32_e32 v48, v61, v48
	v_cvt_pk_f16_f32 v128, v56, v57
	v_cvt_pk_f16_f32 v129, v58, v59
	ds_read_b64_tr_b16 v[152:153], v138 offset:29696
	ds_read_b64_tr_b16 v[154:155], v138 offset:30208
	v_lshl_add_u64 v[228:229], v[188:189], 0, s[22:23]
	v_lshl_add_u64 v[228:229], v[228:229], 0, s[62:63]
	s_add_i32 m0, s30, s64
	s_nop 0
	global_load_lds_dwordx4 v[228:229], off nt
	v_add_f32_e32 v48, v62, v48
	v_add_f32_e32 v48, v63, v48
	v_add_f32_e32 v48, v32, v48
	v_add_f32_e32 v48, v33, v48
	v_cvt_pk_f16_f32 v130, v60, v61
	v_cvt_pk_f16_f32 v131, v62, v63
	ds_read_b64_tr_b16 v[148:149], v138 offset:26624
	ds_read_b64_tr_b16 v[150:151], v138 offset:27136
	v_add_f32_e32 v48, v34, v48
	v_add_f32_e32 v48, v35, v48
	v_add_f32_e32 v48, v36, v48
	v_add_f32_e32 v48, v37, v48
	v_cvt_pk_f16_f32 v124, v32, v33
	v_cvt_pk_f16_f32 v125, v34, v35
	ds_read_b64_tr_b16 v[144:145], v138 offset:30720
	ds_read_b64_tr_b16 v[146:147], v138 offset:31232
	v_lshl_add_u64 v[228:229], v[190:191], 0, s[22:23]
	v_lshl_add_u64 v[228:229], v[228:229], 0, s[62:63]
	s_add_i32 m0, s31, s64
	s_nop 0
	global_load_lds_dwordx4 v[228:229], off nt
	v_add_f32_e32 v32, v38, v48
	v_add_f32_e32 v32, v39, v32
	v_add_f32_e32 v32, v40, v32
	v_add_f32_e32 v32, v41, v32
	v_cvt_pk_f16_f32 v126, v36, v37
	v_cvt_pk_f16_f32 v127, v38, v39
	ds_read_b64_tr_b16 v[140:141], v138 offset:27648
	ds_read_b64_tr_b16 v[142:143], v138 offset:28160
	v_add_f32_e32 v32, v42, v32
	v_add_f32_e32 v32, v43, v32
	v_add_f32_e32 v32, v44, v32
	v_add_f32_e32 v32, v45, v32
	v_cvt_pk_f16_f32 v120, v40, v41
	v_cvt_pk_f16_f32 v121, v42, v43
	ds_read_b64_tr_b16 v[136:137], v138 offset:31744
	ds_read_b64_tr_b16 v[138:139], v138 offset:32256
	v_lshl_add_u64 v[228:229], v[192:193], 0, s[22:23]
	v_lshl_add_u64 v[228:229], v[228:229], 0, s[62:63]
	s_add_i32 m0, s40, s64
	s_nop 0
	global_load_lds_dwordx4 v[228:229], off nt
	v_add_f32_e32 v32, v46, v32
	v_add_f32_e32 v32, v47, v32
	v_add_f32_e32 v108, 0, v32
	v_cvt_pk_f16_f32 v122, v44, v45
	v_cvt_pk_f16_f32 v123, v46, v47
	s_nop 1
	s_nop 0
	v_add_f32_e32 v185, v185, v108
	v_max_f32_e32 v108, v81, v81
	v_max_f32_e32 v109, v80, v80
	v_max_f32_e32 v108, v109, v108
	v_max3_f32 v109, v82, v83, v65
	v_max3_f32 v108, v108, v64, v66
	v_max3_f32 v108, v108, v67, v84
	v_max3_f32 v109, v109, v86, v87
	v_max3_f32 v108, v108, v85, v68
	v_max3_f32 v109, v109, v70, v71
	v_max3_f32 v108, v108, v69, v88
	v_max3_f32 v109, v109, v90, v91
	v_max3_f32 v108, v108, v89, v72
	v_max3_f32 v109, v109, v74, v75
	ds_read_b128 v[48:51], v221 offset:32768
	ds_read_b128 v[32:35], v161 offset:32768
	ds_read_b128 v[52:55], v184 offset:32768
	ds_read_b128 v[36:39], v211 offset:32768
	ds_read_b128 v[56:59], v212 offset:32768
	ds_read_b128 v[40:43], v213 offset:32768
	ds_read_b128 v[60:63], v214 offset:32768
	ds_read_b128 v[44:47], v215 offset:32768
	v_max3_f32 v108, v108, v73, v92
	v_max3_f32 v109, v109, v94, v95
	v_max3_f32 v108, v108, v93, v76
	v_max3_f32 v109, v109, v78, v79
	v_max3_f32 v108, v108, v77, v109
	v_mov_b32_e32 v109, v108
	s_nop 1
	v_permlane32_swap_b32_e32 v108, v109
	v_max_f32_e32 v109, v109, v109
	v_max_f32_e32 v108, v108, v108
	v_max_f32_e32 v108, v108, v109
	v_fma_f32 v108, v108, s39, -v208
	v_cmp_lt_f32_e32 vcc, s46, v108
	s_cmp_lg_u64 vcc, 0
	s_cselect_b64 s[26:27], -1, 0
	s_cbranch_vccnz .LBB3_24

.LBB6_9:
	v_add_u32_e32 v138, s27, v207
	ds_read_b64_tr_b16 v[156:157], v138 offset:24576
	ds_read_b64_tr_b16 v[158:159], v138 offset:25088
	v_add_f32_e32 v120, v80, v81
	s_waitcnt lgkmcnt(3)
	v_mfma_scale_f32_32x32x64_f8f6f4 v[48:63], v[112:119], v[96:103], v[48:63], v219, v220 op_sel_hi:[0,0,0]
	v_add_f32_e32 v112, v82, v120
	v_add_f32_e32 v112, v83, v112
	v_add_f32_e32 v112, v84, v112
	v_add_f32_e32 v116, v85, v112
	v_cvt_pk_f16_f32 v132, v80, v81
	v_cvt_pk_f16_f32 v133, v82, v83
	ds_read_b64_tr_b16 v[112:113], v138 offset:28672
	ds_read_b64_tr_b16 v[114:115], v138 offset:29184
	v_add_f32_e32 v80, v86, v116
	v_add_f32_e32 v80, v87, v80
	v_add_f32_e32 v80, v88, v80
	v_add_f32_e32 v80, v89, v80
	v_cvt_pk_f16_f32 v134, v84, v85
	v_cvt_pk_f16_f32 v135, v86, v87
	s_waitcnt lgkmcnt(4)
	v_mfma_scale_f32_32x32x64_f8f6f4 v[32:47], v[104:111], v[96:103], v[32:47], v219, v220 op_sel_hi:[0,0,0]
	v_lshl_add_u64 v[186:187], v[164:165], 0, s[2:3]
	v_lshl_add_u64 v[228:229], v[186:187], 0, s[10:11]
	v_lshl_add_u64 v[228:229], v[228:229], 0, s[62:63]
	s_add_i32 m0, s38, s65
	s_nop 0
	global_load_lds_dwordx4 v[228:229], off nt
	ds_read_b64_tr_b16 v[104:105], v138 offset:25600
	ds_read_b64_tr_b16 v[106:107], v138 offset:26112
	v_add_f32_e32 v80, v90, v80
	v_add_f32_e32 v80, v91, v80
	v_add_f32_e32 v80, v92, v80
	v_add_f32_e32 v80, v93, v80
	v_cvt_pk_f16_f32 v128, v88, v89
	v_cvt_pk_f16_f32 v129, v90, v91
	ds_read_b64_tr_b16 v[152:153], v138 offset:29696
	ds_read_b64_tr_b16 v[154:155], v138 offset:30208
	v_lshl_add_u64 v[188:189], v[178:179], 0, s[2:3]
	v_lshl_add_u64 v[228:229], v[188:189], 0, s[10:11]
	v_lshl_add_u64 v[228:229], v[228:229], 0, s[62:63]
	s_add_i32 m0, s30, s65
	s_nop 0
	global_load_lds_dwordx4 v[228:229], off nt
	v_add_f32_e32 v80, v94, v80
	v_add_f32_e32 v80, v95, v80
	v_add_f32_e32 v80, v64, v80
	v_add_f32_e32 v80, v65, v80
	v_cvt_pk_f16_f32 v130, v92, v93
	v_cvt_pk_f16_f32 v131, v94, v95
	ds_read_b64_tr_b16 v[148:149], v138 offset:26624
	ds_read_b64_tr_b16 v[150:151], v138 offset:27136
	v_add_f32_e32 v80, v66, v80
	v_add_f32_e32 v80, v67, v80
	v_add_f32_e32 v80, v68, v80
	v_add_f32_e32 v80, v69, v80
	v_cvt_pk_f16_f32 v124, v64, v65
	v_cvt_pk_f16_f32 v125, v66, v67
	ds_read_b64_tr_b16 v[144:145], v138 offset:30720
	ds_read_b64_tr_b16 v[146:147], v138 offset:31232
	v_lshl_add_u64 v[190:191], v[176:177], 0, s[2:3]
	v_lshl_add_u64 v[228:229], v[190:191], 0, s[10:11]
	v_lshl_add_u64 v[228:229], v[228:229], 0, s[62:63]
	s_add_i32 m0, s31, s65
	s_nop 0
	global_load_lds_dwordx4 v[228:229], off nt
	v_add_f32_e32 v64, v70, v80
	v_add_f32_e32 v64, v71, v64
	v_add_f32_e32 v64, v72, v64
	v_add_f32_e32 v64, v73, v64
	v_cvt_pk_f16_f32 v126, v68, v69
	v_cvt_pk_f16_f32 v127, v70, v71
	ds_read_b64_tr_b16 v[140:141], v138 offset:27648
	ds_read_b64_tr_b16 v[142:143], v138 offset:28160
	v_add_f32_e32 v64, v74, v64
	v_add_f32_e32 v64, v75, v64
	v_add_f32_e32 v64, v76, v64
	v_add_f32_e32 v64, v77, v64
	v_cvt_pk_f16_f32 v120, v72, v73
	v_cvt_pk_f16_f32 v121, v74, v75
	ds_read_b64_tr_b16 v[136:137], v138 offset:31744
	ds_read_b64_tr_b16 v[138:139], v138 offset:32256
	v_lshl_add_u64 v[192:193], v[174:175], 0, s[2:3]
	v_lshl_add_u64 v[228:229], v[192:193], 0, s[10:11]
	v_lshl_add_u64 v[228:229], v[228:229], 0, s[62:63]
	s_add_i32 m0, s34, s65
	s_nop 0
	global_load_lds_dwordx4 v[228:229], off nt
	v_add_f32_e32 v64, v78, v64
	v_add_f32_e32 v64, v79, v64
	v_add_f32_e32 v108, 0, v64
	v_cvt_pk_f16_f32 v122, v76, v77
	v_cvt_pk_f16_f32 v123, v78, v79
	s_nop 1
	s_nop 0
	v_add_f32_e32 v185, v185, v108
	v_max_f32_e32 v108, v49, v49
	v_max_f32_e32 v109, v48, v48
	v_max_f32_e32 v108, v109, v108
	v_max3_f32 v109, v50, v51, v33
	v_max3_f32 v108, v108, v32, v34
	v_max3_f32 v108, v108, v35, v52
	v_max3_f32 v109, v109, v54, v55
	v_max3_f32 v108, v108, v53, v36
	v_max3_f32 v109, v109, v38, v39
	v_max3_f32 v108, v108, v37, v56
	v_max3_f32 v109, v109, v58, v59
	v_add_u32_e32 v221, v222, v223
	v_max3_f32 v108, v108, v57, v40
	v_max3_f32 v109, v109, v42, v43
	ds_read_b128 v[80:83], v221
	ds_read_b128 v[64:67], v161
	ds_read_b128 v[84:87], v184
	ds_read_b128 v[68:71], v211
	ds_read_b128 v[88:91], v212
	ds_read_b128 v[72:75], v213
	ds_read_b128 v[92:95], v214
	ds_read_b128 v[76:79], v215
	v_max3_f32 v108, v108, v41, v60
	v_max3_f32 v109, v109, v62, v63
	v_max3_f32 v108, v108, v61, v44
	v_max3_f32 v109, v109, v46, v47
	v_max3_f32 v108, v108, v45, v109
	v_mov_b32_e32 v109, v108
	s_nop 1
	v_permlane32_swap_b32_e32 v108, v109
	v_max_f32_e32 v109, v109, v109
	v_max_f32_e32 v108, v108, v108
	v_max_f32_e32 v108, v108, v109
	v_fma_f32 v108, v108, s41, -v208
	v_cmp_lt_f32_e32 vcc, s29, v108
	s_cmp_lg_u64 vcc, 0
	s_cselect_b64 s[24:25], -1, 0
	s_cbranch_vccnz .LBB6_21

.LBB6_14:
	v_add_u32_e32 v138, s45, v207
	ds_read_b64_tr_b16 v[156:157], v138 offset:24576
	ds_read_b64_tr_b16 v[158:159], v138 offset:25088
	v_add_f32_e32 v120, v48, v49
	s_waitcnt lgkmcnt(4)
	v_mfma_scale_f32_32x32x64_f8f6f4 v[80:95], v[112:119], v[96:103], v[80:95], v219, v220 op_sel_hi:[0,0,0]
	v_add_f32_e32 v112, v50, v120
	v_add_f32_e32 v112, v51, v112
	v_add_f32_e32 v112, v52, v112
	v_add_f32_e32 v116, v53, v112
	v_cvt_pk_f16_f32 v132, v48, v49
	v_cvt_pk_f16_f32 v133, v50, v51
	ds_read_b64_tr_b16 v[112:113], v138 offset:28672
	ds_read_b64_tr_b16 v[114:115], v138 offset:29184
	v_add_f32_e32 v48, v54, v116
	v_add_f32_e32 v48, v55, v48
	v_add_f32_e32 v48, v56, v48
	v_add_f32_e32 v48, v57, v48
	v_cvt_pk_f16_f32 v134, v52, v53
	v_cvt_pk_f16_f32 v135, v54, v55
	s_waitcnt lgkmcnt(4)
	v_mfma_scale_f32_32x32x64_f8f6f4 v[64:79], v[104:111], v[96:103], v[64:79], v219, v220 op_sel_hi:[0,0,0]
	v_lshl_add_u64 v[228:229], v[186:187], 0, s[22:23]
	v_lshl_add_u64 v[228:229], v[228:229], 0, s[62:63]
	s_add_i32 m0, s38, s64
	s_nop 0
	global_load_lds_dwordx4 v[228:229], off nt
	ds_read_b64_tr_b16 v[104:105], v138 offset:25600
	ds_read_b64_tr_b16 v[106:107], v138 offset:26112
	v_add_f32_e32 v48, v58, v48
	v_add_f32_e32 v48, v59, v48
	v_add_f32_e32 v48, v60, v48
	v_add_f32_e32 v48, v61, v48
	v_cvt_pk_f16_f32 v128, v56, v57
	v_cvt_pk_f16_f32 v129, v58, v59
	ds_read_b64_tr_b16 v[152:153], v138 offset:29696
	ds_read_b64_tr_b16 v[154:155], v138 offset:30208
	v_lshl_add_u64 v[228:229], v[188:189], 0, s[22:23]
	v_lshl_add_u64 v[228:229], v[228:229], 0, s[62:63]
	s_add_i32 m0, s30, s64
	s_nop 0
	global_load_lds_dwordx4 v[228:229], off nt
	v_add_f32_e32 v48, v62, v48
	v_add_f32_e32 v48, v63, v48
	v_add_f32_e32 v48, v32, v48
	v_add_f32_e32 v48, v33, v48
	v_cvt_pk_f16_f32 v130, v60, v61
	v_cvt_pk_f16_f32 v131, v62, v63
	ds_read_b64_tr_b16 v[148:149], v138 offset:26624
	ds_read_b64_tr_b16 v[150:151], v138 offset:27136
	v_add_f32_e32 v48, v34, v48
	v_add_f32_e32 v48, v35, v48
	v_add_f32_e32 v48, v36, v48
	v_add_f32_e32 v48, v37, v48
	v_cvt_pk_f16_f32 v124, v32, v33
	v_cvt_pk_f16_f32 v125, v34, v35
	ds_read_b64_tr_b16 v[144:145], v138 offset:30720
	ds_read_b64_tr_b16 v[146:147], v138 offset:31232
	v_lshl_add_u64 v[228:229], v[190:191], 0, s[22:23]
	v_lshl_add_u64 v[228:229], v[228:229], 0, s[62:63]
	s_add_i32 m0, s31, s64
	s_nop 0
	global_load_lds_dwordx4 v[228:229], off nt
	v_add_f32_e32 v32, v38, v48
	v_add_f32_e32 v32, v39, v32
	v_add_f32_e32 v32, v40, v32
	v_add_f32_e32 v32, v41, v32
	v_cvt_pk_f16_f32 v126, v36, v37
	v_cvt_pk_f16_f32 v127, v38, v39
	ds_read_b64_tr_b16 v[140:141], v138 offset:27648
	ds_read_b64_tr_b16 v[142:143], v138 offset:28160
	v_add_f32_e32 v32, v42, v32
	v_add_f32_e32 v32, v43, v32
	v_add_f32_e32 v32, v44, v32
	v_add_f32_e32 v32, v45, v32
	v_cvt_pk_f16_f32 v120, v40, v41
	v_cvt_pk_f16_f32 v121, v42, v43
	ds_read_b64_tr_b16 v[136:137], v138 offset:31744
	ds_read_b64_tr_b16 v[138:139], v138 offset:32256
	v_lshl_add_u64 v[228:229], v[192:193], 0, s[22:23]
	v_lshl_add_u64 v[228:229], v[228:229], 0, s[62:63]
	s_add_i32 m0, s34, s64
	s_nop 0
	global_load_lds_dwordx4 v[228:229], off nt
	v_add_f32_e32 v32, v46, v32
	v_add_f32_e32 v32, v47, v32
	v_add_f32_e32 v108, 0, v32
	v_cvt_pk_f16_f32 v122, v44, v45
	v_cvt_pk_f16_f32 v123, v46, v47
	s_nop 1
	s_nop 0
	v_add_f32_e32 v185, v185, v108
	v_max_f32_e32 v108, v81, v81
	v_max_f32_e32 v109, v80, v80
	v_max_f32_e32 v108, v109, v108
	v_max3_f32 v109, v82, v83, v65
	v_max3_f32 v108, v108, v64, v66
	v_max3_f32 v108, v108, v67, v84
	v_max3_f32 v109, v109, v86, v87
	v_max3_f32 v108, v108, v85, v68
	v_max3_f32 v109, v109, v70, v71
	v_max3_f32 v108, v108, v69, v88
	v_max3_f32 v109, v109, v90, v91
	v_max3_f32 v108, v108, v89, v72
	v_max3_f32 v109, v109, v74, v75
	ds_read_b128 v[48:51], v221 offset:32768
	ds_read_b128 v[32:35], v161 offset:32768
	ds_read_b128 v[52:55], v184 offset:32768
	ds_read_b128 v[36:39], v211 offset:32768
	ds_read_b128 v[56:59], v212 offset:32768
	ds_read_b128 v[40:43], v213 offset:32768
	ds_read_b128 v[60:63], v214 offset:32768
	ds_read_b128 v[44:47], v215 offset:32768
	v_max3_f32 v108, v108, v73, v92
	v_max3_f32 v109, v109, v94, v95
	v_max3_f32 v108, v108, v93, v76
	v_max3_f32 v109, v109, v78, v79
	v_max3_f32 v108, v108, v77, v109
	v_mov_b32_e32 v109, v108
	s_nop 1
	v_permlane32_swap_b32_e32 v108, v109
	v_max_f32_e32 v109, v109, v109
	v_max_f32_e32 v108, v108, v108
	v_max_f32_e32 v108, v108, v109
	v_fma_f32 v108, v108, s41, -v208
	v_cmp_lt_f32_e32 vcc, s29, v108
	s_cmp_lg_u64 vcc, 0
	s_cselect_b64 s[24:25], -1, 0
	s_cbranch_vccnz .LBB6_24
